# P10: next unit's As[1][1] tile-1 DMA issued at the epilogue top (before the scattered stores); peeled first K iteration has no vmcnt wait in its first three sub-phases
# speedup vs baseline: 1.0065x; 1.0065x over previous
; #define PG8_STAGE2(bufoff, gbase, v0, v1) do { \
;         __builtin_amdgcn_global_load_lds((const unsigned*)((const char*)(gbase) + (v0)), (LAS unsigned*)(lds + (bufoff) + ldsw), 16, 0, 0); \
;         __builtin_amdgcn_global_load_lds((const unsigned*)((const char*)(gbase) + (v1)), (LAS unsigned*)(lds + (bufoff) + ldsw + 8192), 16, 0, 0); } while (0)
; #define PG8_STAGE(bufoff, gbase, voff) PG8_STAGE2(bufoff, gbase, (voff)[0], (voff)[1])
; #define PG8_WAIT_V(n) asm volatile("s_waitcnt vmcnt(" #n ")" ::: "memory")
; #define PG8_BAR __builtin_amdgcn_s_barrier()
; template <class Epi, class Sched, bool ALIGN_EPI, bool SP2, bool GATHER>
; DI void gemm_phase(LAS unsigned char* lds, const Gemm g, const Sched& S, const Epi& E) {
;     ...
;     PG8_STAGE(PG8_SB(0, 0), cB, voffB); PG8_STAGE(PG8_SB(0, 1), cB + hstep, voffB); PG8_STAGE2(PG8_SA(0, 0), cA, gC[0][0], gC[0][1]); PG8_STAGE2(PG8_SA(0, 1), cA + hstepA, gC[1][0], gC[1][1]);
;     if (wr == 1) PG8_BAR;
;     PG8_WAIT_V(2); PG8_BAR;
;     PG8_STAGE(PG8_SB(1, 0), cB + kstep, voffB); PG8_STAGE2(PG8_SA(1, 0), cA + kstep, gC[0][0], gC[0][1]); PG8_STAGE(PG8_SB(1, 1), cB + hstep + kstep, voffB);
;     PG8_WAIT_V(6); PG8_BAR;
;     ...
;             const char* a1 = cA + (size_t)(t + 1) * kstep;
.LBB0_990:
	s_waitcnt lgkmcnt(0)
	s_add_u32 s4, s12, 0x240000
	s_addc_u32 s5, s13, 0
	s_add_u32 s6, s10, 0x280000
	s_addc_u32 s7, s11, 0
	s_add_u32 s8, s8, 0x2000000
	s_addc_u32 s9, s9, 0
	s_lshl_b32 s10, s16, 5
	s_and_b32 s16, s10, 0x60
	s_mov_b64 s[10:11], 0x80
	v_lshl_add_u64 v[8:9], v[8:9], 0, s[10:11]
	s_add_i32 m0, s27, 0x18000
	s_lshl_b32 s17, s15, 13
	s_lshl_b32 s18, s16, 7
	s_waitcnt vmcnt(2)
	s_barrier
	global_load_lds_dwordx4 v[8:9], off
	v_lshl_add_u64 v[6:7], v[6:7], 0, s[10:11]
	s_add_i32 m0, s27, 0x1a000
	s_add_i32 s46, s27, 0x8000
	s_add_i32 s47, s27, 0xa000
	global_load_lds_dwordx4 v[6:7], off
	v_lshl_add_u64 v[2:3], v[2:3], 0, s[10:11]
	s_mov_b32 m0, s46
	s_add_u32 s12, s30, 0x20080
	global_load_lds_dwordx4 v[2:3], off
	v_lshl_add_u64 v[2:3], v[4:5], 0, s[10:11]
	s_mov_b32 m0, s47
	s_addc_u32 s13, s31, 0
	global_load_lds_dwordx4 v[2:3], off
	v_lshl_add_u64 v[2:3], s[12:13], 0, v[132:133]
	s_add_i32 m0, s27, 0x1c000
	v_lshlrev_b32_e32 v4, 2, v0
	global_load_lds_dwordx4 v[2:3], off
	v_lshl_add_u64 v[2:3], s[12:13], 0, v[136:137]
	s_add_i32 m0, s27, 0x1e000
	v_lshlrev_b32_e32 v5, 6, v0
	global_load_lds_dwordx4 v[2:3], off
	v_and_b32_e32 v2, 15, v0
	v_lshlrev_b32_e32 v3, 1, v13
	s_movk_i32 s12, 0x3c0
	v_lshl_or_b32 v1, s15, 6, v2
	v_lshl_or_b32 v2, v2, 6, v3
	v_and_b32_e32 v4, 32, v4
	v_and_or_b32 v3, v5, s12, v3
	v_bitop3_b32 v152, s18, v3, v4 bitop3:0xf6
	v_lshlrev_b32_e32 v3, 7, v0
	v_bitop3_b32 v2, v2, s17, v4 bitop3:0xde
	v_and_b32_e32 v3, 0xc000, v3
	v_lshlrev_b32_e32 v4, 10, v12
	v_or3_b32 v3, v10, v3, v4
	v_add_u32_e32 v140, v3, v11
	v_lshlrev_b32_e32 v3, 3, v14
	s_waitcnt vmcnt(6)
	s_cmpk_lt_u32 s14, 0x100
	v_and_b32_e32 v3, 0x1c000, v3
	s_cselect_b64 s[12:13], -1, 0
	v_or3_b32 v3, v10, v3, v4
	s_add_i32 s48, 0, 0x10000
	s_add_i32 s49, 0, 0x14000
	v_or_b32_e32 v153, s16, v13
	v_mov_b32_e32 v141, v139
	v_add_u32_e32 v142, v3, v11
	v_mov_b32_e32 v143, v139
	v_add_u32_e32 v154, s48, v152
	v_add_u32_e32 v155, s49, v152
	v_add_u32_e32 v156, 0, v2
	s_add_u32 s98, s28, 0x20080
	s_addc_u32 s99, s29, 0
	v_lshl_add_u64 v[224:225], s[98:99], 0, v[140:141]
	s_add_i32 m0, s27, 0xc000
	v_lshl_add_u64 v[226:227], s[98:99], 0, v[142:143]
	global_load_lds_dwordx4 v[224:225], off
	s_add_i32 m0, s27, 0xe000
	s_nop 0
	global_load_lds_dwordx4 v[226:227], off
	s_waitcnt vmcnt(0)
	s_barrier
	s_branch .LBB0_993

; #define PG8_STAGE2(bufoff, gbase, v0, v1) do { \
;         __builtin_amdgcn_global_load_lds((const unsigned*)((const char*)(gbase) + (v0)), (LAS unsigned*)(lds + (bufoff) + ldsw), 16, 0, 0); \
;         __builtin_amdgcn_global_load_lds((const unsigned*)((const char*)(gbase) + (v1)), (LAS unsigned*)(lds + (bufoff) + ldsw + 8192), 16, 0, 0); } while (0)
; #define PG8_STAGE(bufoff, gbase, voff) PG8_STAGE2(bufoff, gbase, (voff)[0], (voff)[1])
; #define PG8_WAIT_V(n) asm volatile("s_waitcnt vmcnt(" #n ")" ::: "memory")
; #define PG8_WAIT_L(n) asm volatile("s_waitcnt lgkmcnt(" #n ")" ::: "memory")
; template <class Epi, class Sched, bool ALIGN_EPI, bool SP2, bool GATHER>
; DI void gemm_phase(LAS unsigned char* lds, const Gemm g, const Sched& S, const Epi& E) {
;     ...
;         const bool has_next = S.next(ui + 1, nxt);
;         const char* nA = (has_next && !GATHER) ? (const char*)g.A + (size_t)nxt.pm * tstep : cA; const char* nB = has_next ? (const char*)g.Bt + (size_t)nxt.pn * tstep : cB;
;         if constexpr (GATHER) { if (has_next) { PG8_GATHER(nxt, gN); } else {
; #pragma unroll
;             for (int h = 0; h < 2; ++h) { gN[h][0] = gC[h][0]; gN[h][1] = gC[h][1]; } } }
;         for (int t = 0; t < nt; t += 2) {
;             if constexpr (Epi::MID_T >= 0) { if (t == Epi::MID_T) { E.mid(acc, cur, wr, wc, fr, fq); PG8_SCHED; } }
;             const bool last = (t == nt - 2);
;             const char* a1 = cA + (size_t)(t + 1) * kstep;
;             const char* a2 = last ? nA : cA + (size_t)(t + 2) * kstep; const char* b2 = last ? nB : cB + (size_t)(t + 2) * kstep;
;             const char* a3 = a2 + kstep; const char* b3 = b2 + kstep;
;             unsigned x00 = gC[0][0], x01 = gC[0][1], x10 = gC[1][0], x11 = gC[1][1];
;             if constexpr (GATHER) { if (last) { x00 = gN[0][0]; x01 = gN[0][1]; x10 = gN[1][0]; x11 = gN[1][1]; } }
;             PG8_LDB(B0, 0, 0); PG8_LDB(B1, 0, 1); PG8_SCHED; PG8_LDA(At, 0, 0); PG8_STAGE2(PG8_SA(1, 1), a1 + hstepA, gC[1][0], gC[1][1]);
;             PG8_WAIT_V(8); PG8_WAIT_L(0); PG8_BAR; PG8_MMA(0, 0, At, B0); PG8_MMA(0, 1, At, B1); PG8_BAR; PG8_SCHED;
;             PG8_LDA(At, 0, 1); PG8_STAGE(PG8_SB(0, 0), b2, voffB); PG8_STAGE(PG8_SB(0, 1), b2 + hstep, voffB); PG8_STAGE2(PG8_SA(0, 0), a2, x00, x01);
;             PG8_WAIT_V(8); PG8_WAIT_L(0); PG8_BAR; PG8_MMA(1, 0, At, B0); PG8_MMA(1, 1, At, B1); PG8_BAR; PG8_SCHED;
.LBB0_995:
	s_ashr_i32 s15, s14, 31
	s_lshl_b64 s[20:21], s[14:15], 18
	s_add_u32 s20, s37, s20
	s_addc_u32 s21, s38, s21
	s_and_b64 s[22:23], s[18:19], exec
	s_cselect_b32 s15, s21, s29
	s_cselect_b32 s25, s20, s28
	s_ashr_i32 s17, s16, 31
	s_lshl_b64 s[22:23], s[16:17], 18
	s_add_u32 s22, s39, s22
	s_addc_u32 s23, s40, s23
	s_and_b64 s[34:35], s[18:19], exec
	s_cselect_b32 s17, s23, s31
	s_cselect_b32 s50, s22, s30
	s_add_u32 s28, s28, 0x20080
	s_addc_u32 s29, s29, 0
	s_add_u32 s51, s30, 0x100
	s_addc_u32 s52, s31, 0
	s_mov_b32 s53, -2
	ds_read_b128 v[144:147], v154
	ds_read_b128 v[148:151], v154 offset:1024
	ds_read_b128 v[158:161], v154 offset:2048
	ds_read_b128 v[162:165], v154 offset:3072
	ds_read_b128 v[166:169], v155
	ds_read_b128 v[170:173], v155 offset:1024
	ds_read_b128 v[174:177], v155 offset:2048
	ds_read_b128 v[178:181], v155 offset:3072
	s_add_u32 s30, s28, 0xfffe0080
	s_addc_u32 s31, s29, -1
	s_cmp_eq_u32 s53, 4
	s_cselect_b32 s35, s15, s31
	s_cselect_b32 s34, s25, s30
	s_cselect_b32 s31, s17, s52
	s_cselect_b32 s30, s50, s51
	v_lshl_add_u64 v[214:215], s[28:29], 0, v[140:141]
	s_add_i32 m0, s27, 0xc000
	ds_read_b128 v[182:185], v156
	ds_read_b128 v[186:189], v156 offset:1024
	ds_read_b128 v[190:193], v156 offset:2048
	ds_read_b128 v[194:197], v156 offset:3072
	ds_read_b128 v[198:201], v156 offset:4096
	ds_read_b128 v[202:205], v156 offset:5120
	ds_read_b128 v[206:209], v156 offset:6144
	ds_read_b128 v[210:213], v156 offset:7168
	s_nop 0
	v_lshl_add_u64 v[214:215], s[28:29], 0, v[142:143]
	s_add_i32 m0, s27, 0xe000
	s_nop 0
	s_nop 0
	s_nop 0
	s_waitcnt lgkmcnt(0)
	s_barrier
	s_setprio 1
	s_waitcnt lgkmcnt(0)
	v_mfma_f32_16x16x32_bf16 v[126:129], v[144:147], v[182:185], 0
	v_mfma_f32_16x16x32_bf16 v[122:125], v[158:161], v[182:185], 0
	v_mfma_f32_16x16x32_bf16 v[110:113], v[144:147], v[190:193], 0
	v_mfma_f32_16x16x32_bf16 v[106:109], v[158:161], v[190:193], 0
	v_mfma_f32_16x16x32_bf16 v[94:97], v[144:147], v[198:201], 0
	v_mfma_f32_16x16x32_bf16 v[90:93], v[158:161], v[198:201], 0
	v_mfma_f32_16x16x32_bf16 v[78:81], v[144:147], v[206:209], 0
	v_mfma_f32_16x16x32_bf16 v[74:77], v[158:161], v[206:209], 0
	v_mfma_f32_16x16x32_bf16 v[126:129], v[148:151], v[186:189], v[126:129]
	v_mfma_f32_16x16x32_bf16 v[122:125], v[162:165], v[186:189], v[122:125]
	v_mfma_f32_16x16x32_bf16 v[110:113], v[148:151], v[194:197], v[110:113]
	v_mfma_f32_16x16x32_bf16 v[106:109], v[162:165], v[194:197], v[106:109]
	v_mfma_f32_16x16x32_bf16 v[94:97], v[148:151], v[202:205], v[94:97]
	v_mfma_f32_16x16x32_bf16 v[90:93], v[162:165], v[202:205], v[90:93]
	v_mfma_f32_16x16x32_bf16 v[78:81], v[148:151], v[210:213], v[78:81]
	v_mfma_f32_16x16x32_bf16 v[74:77], v[162:165], v[210:213], v[74:77]
	s_setprio 0
	s_setprio 1
	v_mfma_f32_16x16x32_bf16 v[118:121], v[166:169], v[182:185], 0
	v_mfma_f32_16x16x32_bf16 v[114:117], v[174:177], v[182:185], 0
	v_mfma_f32_16x16x32_bf16 v[102:105], v[166:169], v[190:193], 0
	v_mfma_f32_16x16x32_bf16 v[98:101], v[174:177], v[190:193], 0
	v_mfma_f32_16x16x32_bf16 v[86:89], v[166:169], v[198:201], 0
	v_mfma_f32_16x16x32_bf16 v[82:85], v[174:177], v[198:201], 0
	v_mfma_f32_16x16x32_bf16 v[70:73], v[166:169], v[206:209], 0
	v_mfma_f32_16x16x32_bf16 v[66:69], v[174:177], v[206:209], 0
	v_mfma_f32_16x16x32_bf16 v[118:121], v[170:173], v[186:189], v[118:121]
	v_mfma_f32_16x16x32_bf16 v[114:117], v[178:181], v[186:189], v[114:117]
	v_mfma_f32_16x16x32_bf16 v[102:105], v[170:173], v[194:197], v[102:105]
	v_mfma_f32_16x16x32_bf16 v[98:101], v[178:181], v[194:197], v[98:101]
	v_mfma_f32_16x16x32_bf16 v[86:89], v[170:173], v[202:205], v[86:89]
	v_mfma_f32_16x16x32_bf16 v[82:85], v[178:181], v[202:205], v[82:85]
	v_mfma_f32_16x16x32_bf16 v[70:73], v[170:173], v[210:213], v[70:73]
	v_mfma_f32_16x16x32_bf16 v[66:69], v[178:181], v[210:213], v[66:69]
	s_setprio 0
	s_barrier
	s_add_i32 s54, s48, s41
	v_lshl_add_u64 v[214:215], s[30:31], 0, v[132:133]
	s_mov_b32 m0, s54
	ds_read_b128 v[182:185], v156 offset:16384
	ds_read_b128 v[186:189], v156 offset:17408
	ds_read_b128 v[190:193], v156 offset:18432
	ds_read_b128 v[194:197], v156 offset:19456
	ds_read_b128 v[198:201], v156 offset:20480
	ds_read_b128 v[202:205], v156 offset:21504
	ds_read_b128 v[206:209], v156 offset:22528
	ds_read_b128 v[210:213], v156 offset:23552
	global_load_lds_dwordx4 v[214:215], off
	s_add_i32 m0, s54, 0x2000
	s_add_u32 s54, s30, 0x20000
	v_lshl_add_u64 v[216:217], s[30:31], 0, v[136:137]
	s_addc_u32 s55, s31, 0
	s_add_i32 s56, s49, s41
	global_load_lds_dwordx4 v[216:217], off
	v_lshl_add_u64 v[218:219], s[54:55], 0, v[132:133]
	s_mov_b32 m0, s56
	v_lshl_add_u64 v[220:221], s[34:35], 0, v[134:135]
	global_load_lds_dwordx4 v[218:219], off
	v_lshl_add_u64 v[218:219], s[54:55], 0, v[136:137]
	s_add_i32 m0, s56, 0x2000
	s_nop 0
	global_load_lds_dwordx4 v[218:219], off
	v_lshl_add_u64 v[218:219], s[34:35], 0, v[130:131]
	s_mov_b32 m0, s27
	s_nop 0
	global_load_lds_dwordx4 v[218:219], off
	s_mov_b32 m0, s42
	s_nop 0
	global_load_lds_dwordx4 v[220:221], off
	s_nop 0
	s_waitcnt lgkmcnt(0)
	s_barrier
; #define PG8_STAGE2(bufoff, gbase, v0, v1) do { \
;         __builtin_amdgcn_global_load_lds((const unsigned*)((const char*)(gbase) + (v0)), (LAS unsigned*)(lds + (bufoff) + ldsw), 16, 0, 0); \
;         __builtin_amdgcn_global_load_lds((const unsigned*)((const char*)(gbase) + (v1)), (LAS unsigned*)(lds + (bufoff) + ldsw + 8192), 16, 0, 0); } while (0)
; #define PG8_LDA(dst, b, h) do { _Pragma("unroll") for (int m = 0; m < 4; ++m) _Pragma("unroll") for (int k = 0; k < 2; ++k) dst[m][k] = *(const LAS bf16x8*)(lds + PG8_SA(b, h) + aoff + m * 2048 + k * 1024); } while (0)
; #define PG8_LDB(dst, b, h) do { _Pragma("unroll") for (int n = 0; n < 2; ++n) _Pragma("unroll") for (int k = 0; k < 2; ++k) dst[n][k] = *(const LAS bf16x8*)(lds + PG8_SB(b, h) + boff + n * 2048 + k * 1024); } while (0)
; #define PG8_MMA(ai, bj, At, Bt) do { __builtin_amdgcn_s_setprio(1); _Pragma("unroll") for (int m = 0; m < 4; ++m) _Pragma("unroll") for (int n = 0; n < 2; ++n) _Pragma("unroll") for (int k = 0; k < 2; ++k) \
;         acc[ai][bj][m][n] = __builtin_amdgcn_mfma_f32_16x16x32_bf16(Bt[n][k], At[m][k], acc[ai][bj][m][n], 0, 0, 0); __builtin_amdgcn_s_setprio(0); } while (0)
; #define PG8_WAIT_V(n) asm volatile("s_waitcnt vmcnt(" #n ")" ::: "memory")
; #define PG8_WAIT_L(n) asm volatile("s_waitcnt lgkmcnt(" #n ")" ::: "memory")
; #define PG8_BAR __builtin_amdgcn_s_barrier()
; #define PG8_SCHED __builtin_amdgcn_sched_barrier(0)
; template <class Epi, class Sched, bool ALIGN_EPI, bool SP2, bool GATHER>
; DI void gemm_phase(LAS unsigned char* lds, const Gemm g, const Sched& S, const Epi& E) {
;     ...
;             PG8_WAIT_V(8); PG8_WAIT_L(0); PG8_BAR; PG8_MMA(1, 0, At, B0); PG8_MMA(1, 1, At, B1); PG8_BAR; PG8_SCHED;
;             PG8_LDB(B0, 1, 0); PG8_LDB(B1, 1, 1); PG8_SCHED; PG8_LDA(At, 1, 0); PG8_STAGE2(PG8_SA(0, 1), a2 + hstepA, x10, x11);
;             PG8_WAIT_V(8); PG8_WAIT_L(0); PG8_BAR; PG8_MMA(0, 0, At, B0); PG8_MMA(0, 1, At, B1); PG8_BAR; PG8_SCHED;
	s_setprio 1
	s_waitcnt lgkmcnt(0)
	v_mfma_f32_16x16x32_bf16 v[62:65], v[144:147], v[182:185], 0
	v_mfma_f32_16x16x32_bf16 v[58:61], v[158:161], v[182:185], 0
	v_mfma_f32_16x16x32_bf16 v[46:49], v[144:147], v[190:193], 0
	v_mfma_f32_16x16x32_bf16 v[42:45], v[158:161], v[190:193], 0
	v_mfma_f32_16x16x32_bf16 v[14:17], v[144:147], v[198:201], 0
	v_mfma_f32_16x16x32_bf16 v[10:13], v[158:161], v[198:201], 0
	v_mfma_f32_16x16x32_bf16 v[6:9], v[144:147], v[206:209], 0
	v_mfma_f32_16x16x32_bf16 v[2:5], v[158:161], v[206:209], 0
	v_mfma_f32_16x16x32_bf16 v[62:65], v[148:151], v[186:189], v[62:65]
	v_mfma_f32_16x16x32_bf16 v[58:61], v[162:165], v[186:189], v[58:61]
	v_mfma_f32_16x16x32_bf16 v[46:49], v[148:151], v[194:197], v[46:49]
	v_mfma_f32_16x16x32_bf16 v[42:45], v[162:165], v[194:197], v[42:45]
	v_mfma_f32_16x16x32_bf16 v[14:17], v[148:151], v[202:205], v[14:17]
	v_mfma_f32_16x16x32_bf16 v[10:13], v[162:165], v[202:205], v[10:13]
	v_mfma_f32_16x16x32_bf16 v[6:9], v[148:151], v[210:213], v[6:9]
	v_mfma_f32_16x16x32_bf16 v[2:5], v[162:165], v[210:213], v[2:5]
	s_setprio 0
	s_setprio 1
	v_mfma_f32_16x16x32_bf16 v[54:57], v[166:169], v[182:185], 0
	v_mfma_f32_16x16x32_bf16 v[50:53], v[174:177], v[182:185], 0
	v_mfma_f32_16x16x32_bf16 v[30:33], v[166:169], v[190:193], 0
	v_mfma_f32_16x16x32_bf16 v[26:29], v[174:177], v[190:193], 0
	v_mfma_f32_16x16x32_bf16 v[34:37], v[166:169], v[198:201], 0
	v_mfma_f32_16x16x32_bf16 v[38:41], v[174:177], v[198:201], 0
	v_mfma_f32_16x16x32_bf16 v[18:21], v[166:169], v[206:209], 0
	v_mfma_f32_16x16x32_bf16 v[22:25], v[174:177], v[206:209], 0
	v_mfma_f32_16x16x32_bf16 v[54:57], v[170:173], v[186:189], v[54:57]
	v_mfma_f32_16x16x32_bf16 v[50:53], v[178:181], v[186:189], v[50:53]
	v_mfma_f32_16x16x32_bf16 v[30:33], v[170:173], v[194:197], v[30:33]
	v_mfma_f32_16x16x32_bf16 v[26:29], v[178:181], v[194:197], v[26:29]
	v_mfma_f32_16x16x32_bf16 v[34:37], v[170:173], v[202:205], v[34:37]
	v_mfma_f32_16x16x32_bf16 v[38:41], v[178:181], v[202:205], v[38:41]
	v_mfma_f32_16x16x32_bf16 v[18:21], v[170:173], v[210:213], v[18:21]
	v_mfma_f32_16x16x32_bf16 v[22:25], v[178:181], v[210:213], v[22:25]
	s_setprio 0
	s_barrier
	s_add_i32 s54, 0, 0x18000
	v_add_u32_e32 v138, s54, v152
	s_add_i32 s55, 0, 0x1c000
	ds_read_b128 v[144:147], v138
	ds_read_b128 v[148:151], v138 offset:1024
	ds_read_b128 v[158:161], v138 offset:2048
	ds_read_b128 v[162:165], v138 offset:3072
	v_add_u32_e32 v138, s55, v152
	ds_read_b128 v[166:169], v138
	ds_read_b128 v[170:173], v138 offset:1024
	ds_read_b128 v[174:177], v138 offset:2048
	ds_read_b128 v[178:181], v138 offset:3072
	s_add_u32 s34, s34, 0x20000
	s_addc_u32 s35, s35, 0
	s_mov_b32 m0, s43
	v_lshl_add_u64 v[222:223], s[34:35], 0, v[130:131]
	ds_read_b128 v[182:185], v156 offset:32768
	ds_read_b128 v[186:189], v156 offset:33792
	ds_read_b128 v[190:193], v156 offset:34816
	ds_read_b128 v[194:197], v156 offset:35840
	ds_read_b128 v[198:201], v156 offset:36864
	ds_read_b128 v[202:205], v156 offset:37888
	ds_read_b128 v[206:209], v156 offset:38912
	ds_read_b128 v[210:213], v156 offset:39936
	global_load_lds_dwordx4 v[222:223], off
	v_lshl_add_u64 v[222:223], s[34:35], 0, v[134:135]
	s_mov_b32 m0, s44
	s_nop 0
	global_load_lds_dwordx4 v[222:223], off
	s_nop 0
	s_waitcnt lgkmcnt(0)
	s_barrier
	s_setprio 1
	s_waitcnt lgkmcnt(0)
	v_mfma_f32_16x16x32_bf16 v[126:129], v[144:147], v[182:185], v[126:129]
	v_mfma_f32_16x16x32_bf16 v[122:125], v[158:161], v[182:185], v[122:125]
	v_mfma_f32_16x16x32_bf16 v[110:113], v[144:147], v[190:193], v[110:113]
	v_mfma_f32_16x16x32_bf16 v[106:109], v[158:161], v[190:193], v[106:109]
	v_mfma_f32_16x16x32_bf16 v[94:97], v[144:147], v[198:201], v[94:97]
	v_mfma_f32_16x16x32_bf16 v[90:93], v[158:161], v[198:201], v[90:93]
	v_mfma_f32_16x16x32_bf16 v[78:81], v[144:147], v[206:209], v[78:81]
	v_mfma_f32_16x16x32_bf16 v[74:77], v[158:161], v[206:209], v[74:77]
	v_mfma_f32_16x16x32_bf16 v[126:129], v[148:151], v[186:189], v[126:129]
	v_mfma_f32_16x16x32_bf16 v[122:125], v[162:165], v[186:189], v[122:125]
	v_mfma_f32_16x16x32_bf16 v[110:113], v[148:151], v[194:197], v[110:113]
	v_mfma_f32_16x16x32_bf16 v[106:109], v[162:165], v[194:197], v[106:109]
	v_mfma_f32_16x16x32_bf16 v[94:97], v[148:151], v[202:205], v[94:97]
	v_mfma_f32_16x16x32_bf16 v[90:93], v[162:165], v[202:205], v[90:93]
	v_mfma_f32_16x16x32_bf16 v[78:81], v[148:151], v[210:213], v[78:81]
	v_mfma_f32_16x16x32_bf16 v[74:77], v[162:165], v[210:213], v[74:77]
	s_setprio 0
	s_setprio 1
	v_mfma_f32_16x16x32_bf16 v[118:121], v[166:169], v[182:185], v[118:121]
	v_mfma_f32_16x16x32_bf16 v[114:117], v[174:177], v[182:185], v[114:117]
	v_mfma_f32_16x16x32_bf16 v[102:105], v[166:169], v[190:193], v[102:105]
	v_mfma_f32_16x16x32_bf16 v[98:101], v[174:177], v[190:193], v[98:101]
	v_mfma_f32_16x16x32_bf16 v[86:89], v[166:169], v[198:201], v[86:89]
	v_mfma_f32_16x16x32_bf16 v[82:85], v[174:177], v[198:201], v[82:85]
	v_mfma_f32_16x16x32_bf16 v[70:73], v[166:169], v[206:209], v[70:73]
	v_mfma_f32_16x16x32_bf16 v[66:69], v[174:177], v[206:209], v[66:69]
	v_mfma_f32_16x16x32_bf16 v[118:121], v[170:173], v[186:189], v[118:121]
	v_mfma_f32_16x16x32_bf16 v[114:117], v[178:181], v[186:189], v[114:117]
	v_mfma_f32_16x16x32_bf16 v[102:105], v[170:173], v[194:197], v[102:105]
	v_mfma_f32_16x16x32_bf16 v[98:101], v[178:181], v[194:197], v[98:101]
	v_mfma_f32_16x16x32_bf16 v[86:89], v[170:173], v[202:205], v[86:89]
	v_mfma_f32_16x16x32_bf16 v[82:85], v[178:181], v[202:205], v[82:85]
	v_mfma_f32_16x16x32_bf16 v[70:73], v[170:173], v[210:213], v[70:73]
	v_mfma_f32_16x16x32_bf16 v[66:69], v[178:181], v[210:213], v[66:69]
	s_setprio 0
	s_barrier
; #define PG8_STAGE2(bufoff, gbase, v0, v1) do { \
;         __builtin_amdgcn_global_load_lds((const unsigned*)((const char*)(gbase) + (v0)), (LAS unsigned*)(lds + (bufoff) + ldsw), 16, 0, 0); \
;         __builtin_amdgcn_global_load_lds((const unsigned*)((const char*)(gbase) + (v1)), (LAS unsigned*)(lds + (bufoff) + ldsw + 8192), 16, 0, 0); } while (0)
; #define PG8_STAGE(bufoff, gbase, voff) PG8_STAGE2(bufoff, gbase, (voff)[0], (voff)[1])
; #define PG8_LDA(dst, b, h) do { _Pragma("unroll") for (int m = 0; m < 4; ++m) _Pragma("unroll") for (int k = 0; k < 2; ++k) dst[m][k] = *(const LAS bf16x8*)(lds + PG8_SA(b, h) + aoff + m * 2048 + k * 1024); } while (0)
; #define PG8_MMA(ai, bj, At, Bt) do { __builtin_amdgcn_s_setprio(1); _Pragma("unroll") for (int m = 0; m < 4; ++m) _Pragma("unroll") for (int n = 0; n < 2; ++n) _Pragma("unroll") for (int k = 0; k < 2; ++k) \
;         acc[ai][bj][m][n] = __builtin_amdgcn_mfma_f32_16x16x32_bf16(Bt[n][k], At[m][k], acc[ai][bj][m][n], 0, 0, 0); __builtin_amdgcn_s_setprio(0); } while (0)
; #define PG8_WAIT_V(n) asm volatile("s_waitcnt vmcnt(" #n ")" ::: "memory")
; #define PG8_WAIT_L(n) asm volatile("s_waitcnt lgkmcnt(" #n ")" ::: "memory")
; #define PG8_BAR __builtin_amdgcn_s_barrier()
; #define PG8_SCHED __builtin_amdgcn_sched_barrier(0)
; template <class Epi, class Sched, bool ALIGN_EPI, bool SP2, bool GATHER>
; DI void gemm_phase(LAS unsigned char* lds, const Gemm g, const Sched& S, const Epi& E) {
;     ...
;             PG8_LDA(At, 1, 1); PG8_STAGE(PG8_SB(1, 0), b3, voffB); PG8_STAGE(PG8_SB(1, 1), b3 + hstep, voffB); PG8_STAGE2(PG8_SA(1, 0), a3, x00, x01);
;             PG8_WAIT_V(8); PG8_WAIT_L(0); PG8_BAR; PG8_MMA(1, 0, At, B0); PG8_MMA(1, 1, At, B1); PG8_BAR; PG8_SCHED;
;         }
	s_add_i32 s34, s54, s41
	v_lshl_add_u64 v[214:215], v[214:215], 0, s[10:11]
	s_mov_b32 m0, s34
	ds_read_b128 v[182:185], v156 offset:49152
	ds_read_b128 v[186:189], v156 offset:50176
	ds_read_b128 v[190:193], v156 offset:51200
	ds_read_b128 v[194:197], v156 offset:52224
	ds_read_b128 v[198:201], v156 offset:53248
	ds_read_b128 v[202:205], v156 offset:54272
	ds_read_b128 v[206:209], v156 offset:55296
	ds_read_b128 v[210:213], v156 offset:56320
	global_load_lds_dwordx4 v[214:215], off
	s_add_i32 m0, s34, 0x2000
	s_add_u32 s30, s30, 0x20080
	v_lshl_add_u64 v[214:215], v[216:217], 0, s[10:11]
	s_addc_u32 s31, s31, 0
	s_add_i32 s34, s55, s41
	global_load_lds_dwordx4 v[214:215], off
	v_lshl_add_u64 v[214:215], s[30:31], 0, v[132:133]
	s_mov_b32 m0, s34
	s_nop 0
	global_load_lds_dwordx4 v[214:215], off
	v_lshl_add_u64 v[214:215], s[30:31], 0, v[136:137]
	s_add_i32 m0, s34, 0x2000
	s_nop 0
	global_load_lds_dwordx4 v[214:215], off
	v_lshl_add_u64 v[214:215], v[218:219], 0, s[10:11]
	s_mov_b32 m0, s46
	s_nop 0
	global_load_lds_dwordx4 v[214:215], off
	v_lshl_add_u64 v[214:215], v[220:221], 0, s[10:11]
	s_mov_b32 m0, s47
	s_nop 0
	global_load_lds_dwordx4 v[214:215], off
	s_waitcnt vmcnt(8)
	s_waitcnt lgkmcnt(0)
	s_barrier
	s_setprio 1
	s_waitcnt lgkmcnt(0)
	v_mfma_f32_16x16x32_bf16 v[62:65], v[144:147], v[182:185], v[62:65]
	v_mfma_f32_16x16x32_bf16 v[58:61], v[158:161], v[182:185], v[58:61]
	v_mfma_f32_16x16x32_bf16 v[46:49], v[144:147], v[190:193], v[46:49]
	v_mfma_f32_16x16x32_bf16 v[42:45], v[158:161], v[190:193], v[42:45]
	v_mfma_f32_16x16x32_bf16 v[14:17], v[144:147], v[198:201], v[14:17]
	v_mfma_f32_16x16x32_bf16 v[10:13], v[158:161], v[198:201], v[10:13]
	v_mfma_f32_16x16x32_bf16 v[6:9], v[144:147], v[206:209], v[6:9]
	v_mfma_f32_16x16x32_bf16 v[2:5], v[158:161], v[206:209], v[2:5]
	v_mfma_f32_16x16x32_bf16 v[62:65], v[148:151], v[186:189], v[62:65]
	v_mfma_f32_16x16x32_bf16 v[58:61], v[162:165], v[186:189], v[58:61]
	v_mfma_f32_16x16x32_bf16 v[46:49], v[148:151], v[194:197], v[46:49]
	v_mfma_f32_16x16x32_bf16 v[42:45], v[162:165], v[194:197], v[42:45]
	v_mfma_f32_16x16x32_bf16 v[14:17], v[148:151], v[202:205], v[14:17]
	v_mfma_f32_16x16x32_bf16 v[10:13], v[162:165], v[202:205], v[10:13]
	v_mfma_f32_16x16x32_bf16 v[6:9], v[148:151], v[210:213], v[6:9]
	v_mfma_f32_16x16x32_bf16 v[2:5], v[162:165], v[210:213], v[2:5]
	s_setprio 0
	s_setprio 1
	v_mfma_f32_16x16x32_bf16 v[54:57], v[166:169], v[182:185], v[54:57]
	v_mfma_f32_16x16x32_bf16 v[50:53], v[174:177], v[182:185], v[50:53]
	v_mfma_f32_16x16x32_bf16 v[30:33], v[166:169], v[190:193], v[30:33]
	v_mfma_f32_16x16x32_bf16 v[26:29], v[174:177], v[190:193], v[26:29]
	v_mfma_f32_16x16x32_bf16 v[34:37], v[166:169], v[198:201], v[34:37]
	v_mfma_f32_16x16x32_bf16 v[38:41], v[174:177], v[198:201], v[38:41]
	v_mfma_f32_16x16x32_bf16 v[18:21], v[166:169], v[206:209], v[18:21]
	v_mfma_f32_16x16x32_bf16 v[22:25], v[174:177], v[206:209], v[22:25]
	v_mfma_f32_16x16x32_bf16 v[54:57], v[170:173], v[186:189], v[54:57]
	v_mfma_f32_16x16x32_bf16 v[50:53], v[178:181], v[186:189], v[50:53]
	v_mfma_f32_16x16x32_bf16 v[30:33], v[170:173], v[194:197], v[30:33]
	v_mfma_f32_16x16x32_bf16 v[26:29], v[178:181], v[194:197], v[26:29]
	v_mfma_f32_16x16x32_bf16 v[34:37], v[170:173], v[202:205], v[34:37]
	v_mfma_f32_16x16x32_bf16 v[38:41], v[178:181], v[202:205], v[38:41]
	v_mfma_f32_16x16x32_bf16 v[18:21], v[170:173], v[210:213], v[18:21]
	v_mfma_f32_16x16x32_bf16 v[22:25], v[178:181], v[210:213], v[22:25]
	s_setprio 0
	s_barrier
	s_add_i32 s53, s53, 2
	s_add_u32 s28, s28, 0x100
	s_addc_u32 s29, s29, 0
	s_add_u32 s51, s51, 0x100
	s_addc_u32 s52, s52, 0
	s_cmp_gt_u32 s53, 5
	s_cbranch_scc1 .Lpeel_exit_p10

; DI unsigned cvt_pk_bf16(float lo, float hi) { unsigned r; asm volatile("v_cvt_pk_bf16_f32 %0, %1, %2" : "=v"(r) : "v"(lo), "v"(hi)); return r; }
; template <class Epi, class Sched, bool ALIGN_EPI, bool SP2, bool GATHER>
; DI void gemm_phase(LAS unsigned char* lds, const Gemm g, const Sched& S, const Epi& E) {
;     ...
;             const char* a1 = cA + (size_t)(t + 1) * kstep;
;     DI void operator()(const f32x4 (&acc)[2][2][4][2], const pg8::Unit& u, int wr, int wc, int fr, int fq) const {
;         const int row0 = u.pm * 256 + wr * 64 + fr, col0 = (u.pn & 7) * 256 + wc * 32 + 8 * fq;
; #pragma unroll
;         for (int ai = 0; ai < 2; ++ai)
; #pragma unroll
;             for (int m = 0; m < 4; ++m) {
;                 const int p = row0 + ai * 128 + m * 16; const int dst = rowdst[p]; const float w = roww[p];
;                 if (dst >= 0) {
; #pragma unroll
;                     for (int bj = 0; bj < 2; ++bj) {
;                         const f32x4 a0 = acc[ai][bj][m][0] * w, a1 = acc[ai][bj][m][1] * w;
;                         u32x4 o; o.x = pg8::cvt_pk_bf16(a0[0], a0[1]); o.y = pg8::cvt_pk_bf16(a0[2], a0[3]); o.z = pg8::cvt_pk_bf16(a1[0], a1[1]); o.w = pg8::cvt_pk_bf16(a1[2], a1[3]);
;                         *(u32x4*)(YK + (size_t)dst * D + col0 + bj * 128) = o;
;                     }
;                 }
;             }
;     }
.LBB0_999:
	s_add_u32 s98, s20, 0x20080
	s_addc_u32 s99, s21, 0
	v_lshl_add_u64 v[224:225], s[98:99], 0, v[140:141]
	s_add_i32 m0, s27, 0xc000
	v_lshl_add_u64 v[226:227], s[98:99], 0, v[142:143]
	global_load_lds_dwordx4 v[224:225], off
	s_add_i32 m0, s27, 0xe000
	s_nop 0
	global_load_lds_dwordx4 v[226:227], off
	v_lshl_add_u32 v164, s26, 8, v1
	v_ashrrev_i32_e32 v165, 31, v164
	v_lshl_add_u64 v[166:167], v[164:165], 2, s[4:5]
	global_load_dword v176, v[166:167], off
	v_mov_b32_e32 v177, v139
	v_lshl_add_u64 v[168:169], v[164:165], 2, s[6:7]
	global_load_dword v178, v[168:169], off
	v_or_b32_e32 v170, 16, v164
	v_ashrrev_i32_e32 v171, 31, v170
	v_lshl_add_u64 v[172:173], v[170:171], 2, s[4:5]
	global_load_dword v180, v[172:173], off
	v_mov_b32_e32 v181, v139
	v_lshl_add_u64 v[172:173], v[170:171], 2, s[6:7]
	global_load_dword v182, v[172:173], off
	v_or_b32_e32 v170, 32, v164
	v_ashrrev_i32_e32 v171, 31, v170
	v_lshl_add_u64 v[172:173], v[170:171], 2, s[4:5]
	global_load_dword v184, v[172:173], off
	v_mov_b32_e32 v185, v139
	v_lshl_add_u64 v[172:173], v[170:171], 2, s[6:7]
	global_load_dword v186, v[172:173], off
	v_or_b32_e32 v170, 48, v164
	v_ashrrev_i32_e32 v171, 31, v170
	v_lshl_add_u64 v[164:165], v[170:171], 2, s[4:5]
	global_load_dword v188, v[164:165], off
	v_mov_b32_e32 v189, v139
	v_lshl_add_u64 v[164:165], v[170:171], 2, s[6:7]
	global_load_dword v190, v[164:165], off
	global_load_dword v192, v[166:167], off offset:512
	v_mov_b32_e32 v193, v139
	global_load_dword v194, v[168:169], off offset:512
	global_load_dword v196, v[166:167], off offset:576
	v_mov_b32_e32 v197, v139
	global_load_dword v198, v[168:169], off offset:576
	global_load_dword v200, v[166:167], off offset:640
	v_mov_b32_e32 v201, v139
	global_load_dword v202, v[168:169], off offset:640
	global_load_dword v204, v[166:167], off offset:704
	v_mov_b32_e32 v205, v139
	global_load_dword v206, v[168:169], off offset:704
	s_waitcnt vmcnt(0)
	v_lshl_add_u32 v150, s26, 8, v1
	v_ashrrev_i32_e32 v151, 31, v150
	v_lshl_add_u64 v[148:149], v[150:151], 2, s[4:5]
	s_nop 0
	s_lshl_b32 s15, s24, 8
	s_and_b32 s15, s15, 0x700
	v_or_b32_e32 v144, s15, v153
	v_lshl_add_u64 v[146:147], v[150:151], 2, s[6:7]
	v_lshlrev_b32_e32 v144, 1, v144
	s_nop 0
	v_cmp_lt_i32_e32 vcc, -1, v176
	s_and_saveexec_b64 s[24:25], vcc
	s_nop 0
	v_lshlrev_b64 v[160:161], 12, v[176:177]
	v_mov_b32_e32 v145, v139
	v_lshl_add_u64 v[160:161], s[8:9], 0, v[160:161]
	v_lshl_add_u64 v[160:161], v[160:161], 0, v[144:145]
	s_nop 0
	v_pk_mul_f32 v[128:129], v[128:129], v[178:179] op_sel_hi:[1,0]
	v_pk_mul_f32 v[126:127], v[126:127], v[178:179] op_sel_hi:[1,0]
	v_pk_mul_f32 v[124:125], v[124:125], v[178:179] op_sel_hi:[1,0]
	v_pk_mul_f32 v[122:123], v[122:123], v[178:179] op_sel_hi:[1,0]
	v_pk_mul_f32 v[120:121], v[120:121], v[178:179] op_sel_hi:[1,0]
	v_pk_mul_f32 v[118:119], v[118:119], v[178:179] op_sel_hi:[1,0]
	v_pk_mul_f32 v[162:163], v[116:117], v[178:179] op_sel_hi:[1,0]
	v_pk_mul_f32 v[158:159], v[114:115], v[178:179] op_sel_hi:[1,0]
	v_cvt_pk_bf16_f32 v114, v126, v127
	v_cvt_pk_bf16_f32 v115, v128, v129
	v_cvt_pk_bf16_f32 v116, v122, v123
	v_cvt_pk_bf16_f32 v117, v124, v125
	global_store_dwordx4 v[160:161], v[114:117], off
	s_nop 1
	v_cvt_pk_bf16_f32 v114, v118, v119
	v_cvt_pk_bf16_f32 v115, v120, v121
	v_cvt_pk_bf16_f32 v116, v158, v159
	v_cvt_pk_bf16_f32 v117, v162, v163
	global_store_dwordx4 v[160:161], v[114:117], off offset:256
	s_or_b64 exec, exec, s[24:25]
	s_nop 0
	v_or_b32_e32 v114, 16, v150
	v_ashrrev_i32_e32 v115, 31, v114
	v_lshl_add_u64 v[116:117], v[114:115], 2, s[4:5]
	s_nop 0
	s_nop 0
	v_cmp_lt_i32_e32 vcc, -1, v180
	s_and_saveexec_b64 s[24:25], vcc
	v_lshl_add_u64 v[114:115], v[114:115], 2, s[6:7]
	s_nop 0
	v_lshlrev_b64 v[116:117], 12, v[180:181]
	v_mov_b32_e32 v145, v139
	v_lshl_add_u64 v[116:117], s[8:9], 0, v[116:117]
	v_lshl_add_u64 v[116:117], v[116:117], 0, v[144:145]
	s_nop 0
	v_pk_mul_f32 v[112:113], v[112:113], v[182:183] op_sel_hi:[1,0]
	v_pk_mul_f32 v[110:111], v[110:111], v[182:183] op_sel_hi:[1,0]
	v_pk_mul_f32 v[108:109], v[108:109], v[182:183] op_sel_hi:[1,0]
	v_pk_mul_f32 v[106:107], v[106:107], v[182:183] op_sel_hi:[1,0]
	v_pk_mul_f32 v[104:105], v[104:105], v[182:183] op_sel_hi:[1,0]
	v_pk_mul_f32 v[102:103], v[102:103], v[182:183] op_sel_hi:[1,0]
	v_pk_mul_f32 v[118:119], v[100:101], v[182:183] op_sel_hi:[1,0]
	v_pk_mul_f32 v[114:115], v[98:99], v[182:183] op_sel_hi:[1,0]
	v_cvt_pk_bf16_f32 v98, v110, v111
	v_cvt_pk_bf16_f32 v99, v112, v113
	v_cvt_pk_bf16_f32 v100, v106, v107
	v_cvt_pk_bf16_f32 v101, v108, v109
	global_store_dwordx4 v[116:117], v[98:101], off
	s_nop 1
	v_cvt_pk_bf16_f32 v98, v102, v103
	v_cvt_pk_bf16_f32 v99, v104, v105
	v_cvt_pk_bf16_f32 v100, v114, v115
	v_cvt_pk_bf16_f32 v101, v118, v119
	global_store_dwordx4 v[116:117], v[98:101], off offset:256
	s_or_b64 exec, exec, s[24:25]
	s_nop 0
	v_or_b32_e32 v98, 32, v150
	v_ashrrev_i32_e32 v99, 31, v98
	v_lshl_add_u64 v[100:101], v[98:99], 2, s[4:5]
	s_nop 0
	s_nop 0
	v_cmp_lt_i32_e32 vcc, -1, v184
	s_and_saveexec_b64 s[24:25], vcc
	v_lshl_add_u64 v[98:99], v[98:99], 2, s[6:7]
	s_nop 0
	v_lshlrev_b64 v[100:101], 12, v[184:185]
	v_mov_b32_e32 v145, v139
	v_lshl_add_u64 v[100:101], s[8:9], 0, v[100:101]
	v_lshl_add_u64 v[100:101], v[100:101], 0, v[144:145]
	s_nop 0
	v_pk_mul_f32 v[96:97], v[96:97], v[186:187] op_sel_hi:[1,0]
	v_pk_mul_f32 v[94:95], v[94:95], v[186:187] op_sel_hi:[1,0]
	v_pk_mul_f32 v[92:93], v[92:93], v[186:187] op_sel_hi:[1,0]
	v_pk_mul_f32 v[90:91], v[90:91], v[186:187] op_sel_hi:[1,0]
	v_pk_mul_f32 v[88:89], v[88:89], v[186:187] op_sel_hi:[1,0]
	v_pk_mul_f32 v[86:87], v[86:87], v[186:187] op_sel_hi:[1,0]
; DI unsigned cvt_pk_bf16(float lo, float hi) { unsigned r; asm volatile("v_cvt_pk_bf16_f32 %0, %1, %2" : "=v"(r) : "v"(lo), "v"(hi)); return r; }
; #define PG8_BAR __builtin_amdgcn_s_barrier()
; template <class Epi, class Sched, bool ALIGN_EPI, bool SP2, bool GATHER>
; DI void gemm_phase(LAS unsigned char* lds, const Gemm g, const Sched& S, const Epi& E) {
;     ...
;         if (!has_next) break;
; #pragma unroll
;         for (int a = 0; a < 2; ++a)
; #pragma unroll
;             for (int b = 0; b < 2; ++b)
; #pragma unroll
;                 for (int m = 0; m < 4; ++m)
; #pragma unroll
;                     for (int n = 0; n < 2; ++n) acc[a][b][m][n] = (f32x4){0.f, 0.f, 0.f, 0.f};
;         cur = nxt; cA = nA; cB = nB; ++ui;
; #pragma unroll
;         for (int h = 0; h < 2; ++h) { gC[h][0] = gN[h][0]; gC[h][1] = gN[h][1]; }
;         if constexpr (ALIGN_EPI) { if (wr == 1) PG8_BAR; }
;     DI void operator()(const f32x4 (&acc)[2][2][4][2], const pg8::Unit& u, int wr, int wc, int fr, int fq) const {
;     ...
;                 const int p = row0 + ai * 128 + m * 16; const int dst = rowdst[p]; const float w = roww[p];
;                 if (dst >= 0) {
; #pragma unroll
;                     for (int bj = 0; bj < 2; ++bj) {
;                         const f32x4 a0 = acc[ai][bj][m][0] * w, a1 = acc[ai][bj][m][1] * w;
;                         u32x4 o; o.x = pg8::cvt_pk_bf16(a0[0], a0[1]); o.y = pg8::cvt_pk_bf16(a0[2], a0[3]); o.z = pg8::cvt_pk_bf16(a1[0], a1[1]); o.w = pg8::cvt_pk_bf16(a1[2], a1[3]);
;                         *(u32x4*)(YK + (size_t)dst * D + col0 + bj * 128) = o;
;                     }
;                 }
;             }
;     }
	v_pk_mul_f32 v[102:103], v[84:85], v[186:187] op_sel_hi:[1,0]
	v_pk_mul_f32 v[98:99], v[82:83], v[186:187] op_sel_hi:[1,0]
	v_cvt_pk_bf16_f32 v82, v94, v95
	v_cvt_pk_bf16_f32 v83, v96, v97
	v_cvt_pk_bf16_f32 v84, v90, v91
	v_cvt_pk_bf16_f32 v85, v92, v93
	global_store_dwordx4 v[100:101], v[82:85], off
	s_nop 1
	v_cvt_pk_bf16_f32 v82, v86, v87
	v_cvt_pk_bf16_f32 v83, v88, v89
	v_cvt_pk_bf16_f32 v84, v98, v99
	v_cvt_pk_bf16_f32 v85, v102, v103
	global_store_dwordx4 v[100:101], v[82:85], off offset:256
	s_or_b64 exec, exec, s[24:25]
	s_nop 0
	v_or_b32_e32 v82, 48, v150
	v_ashrrev_i32_e32 v83, 31, v82
	v_lshl_add_u64 v[84:85], v[82:83], 2, s[4:5]
	s_nop 0
	s_nop 0
	v_cmp_lt_i32_e32 vcc, -1, v188
	s_and_saveexec_b64 s[24:25], vcc
	v_lshl_add_u64 v[82:83], v[82:83], 2, s[6:7]
	s_nop 0
	v_lshlrev_b64 v[84:85], 12, v[188:189]
	v_mov_b32_e32 v145, v139
	v_lshl_add_u64 v[84:85], s[8:9], 0, v[84:85]
	v_lshl_add_u64 v[84:85], v[84:85], 0, v[144:145]
	s_nop 0
	v_pk_mul_f32 v[80:81], v[80:81], v[190:191] op_sel_hi:[1,0]
	v_pk_mul_f32 v[78:79], v[78:79], v[190:191] op_sel_hi:[1,0]
	v_pk_mul_f32 v[76:77], v[76:77], v[190:191] op_sel_hi:[1,0]
	v_pk_mul_f32 v[74:75], v[74:75], v[190:191] op_sel_hi:[1,0]
	v_pk_mul_f32 v[72:73], v[72:73], v[190:191] op_sel_hi:[1,0]
	v_pk_mul_f32 v[70:71], v[70:71], v[190:191] op_sel_hi:[1,0]
	v_pk_mul_f32 v[86:87], v[68:69], v[190:191] op_sel_hi:[1,0]
	v_pk_mul_f32 v[82:83], v[66:67], v[190:191] op_sel_hi:[1,0]
	v_cvt_pk_bf16_f32 v66, v78, v79
	v_cvt_pk_bf16_f32 v67, v80, v81
	v_cvt_pk_bf16_f32 v68, v74, v75
	v_cvt_pk_bf16_f32 v69, v76, v77
	global_store_dwordx4 v[84:85], v[66:69], off
	s_nop 1
	v_cvt_pk_bf16_f32 v66, v70, v71
	v_cvt_pk_bf16_f32 v67, v72, v73
	v_cvt_pk_bf16_f32 v68, v82, v83
	v_cvt_pk_bf16_f32 v69, v86, v87
	global_store_dwordx4 v[84:85], v[66:69], off offset:256
	s_or_b64 exec, exec, s[24:25]
	s_nop 0
	s_nop 0
	v_cmp_lt_i32_e32 vcc, -1, v192
	s_and_saveexec_b64 s[24:25], vcc
	s_nop 0
	v_lshlrev_b64 v[68:69], 12, v[192:193]
	v_mov_b32_e32 v145, v139
	v_lshl_add_u64 v[68:69], s[8:9], 0, v[68:69]
	v_lshl_add_u64 v[68:69], v[68:69], 0, v[144:145]
	s_nop 0
	v_pk_mul_f32 v[64:65], v[64:65], v[194:195] op_sel_hi:[1,0]
	v_pk_mul_f32 v[62:63], v[62:63], v[194:195] op_sel_hi:[1,0]
	v_pk_mul_f32 v[60:61], v[60:61], v[194:195] op_sel_hi:[1,0]
	v_pk_mul_f32 v[58:59], v[58:59], v[194:195] op_sel_hi:[1,0]
	v_pk_mul_f32 v[56:57], v[56:57], v[194:195] op_sel_hi:[1,0]
	v_pk_mul_f32 v[54:55], v[54:55], v[194:195] op_sel_hi:[1,0]
	v_pk_mul_f32 v[70:71], v[52:53], v[194:195] op_sel_hi:[1,0]
	v_pk_mul_f32 v[66:67], v[50:51], v[194:195] op_sel_hi:[1,0]
	v_cvt_pk_bf16_f32 v50, v62, v63
	v_cvt_pk_bf16_f32 v51, v64, v65
	v_cvt_pk_bf16_f32 v52, v58, v59
	v_cvt_pk_bf16_f32 v53, v60, v61
	global_store_dwordx4 v[68:69], v[50:53], off
	s_nop 1
	v_cvt_pk_bf16_f32 v50, v54, v55
	v_cvt_pk_bf16_f32 v51, v56, v57
	v_cvt_pk_bf16_f32 v52, v66, v67
	v_cvt_pk_bf16_f32 v53, v70, v71
	global_store_dwordx4 v[68:69], v[50:53], off offset:256
	s_or_b64 exec, exec, s[24:25]
	s_nop 0
	s_nop 0
	v_cmp_lt_i32_e32 vcc, -1, v196
	s_and_saveexec_b64 s[24:25], vcc
	s_nop 0
	v_lshlrev_b64 v[52:53], 12, v[196:197]
	v_mov_b32_e32 v145, v139
	v_lshl_add_u64 v[52:53], s[8:9], 0, v[52:53]
	v_lshl_add_u64 v[52:53], v[52:53], 0, v[144:145]
	s_nop 0
	v_pk_mul_f32 v[48:49], v[48:49], v[198:199] op_sel_hi:[1,0]
	v_pk_mul_f32 v[46:47], v[46:47], v[198:199] op_sel_hi:[1,0]
	v_pk_mul_f32 v[44:45], v[44:45], v[198:199] op_sel_hi:[1,0]
	v_pk_mul_f32 v[42:43], v[42:43], v[198:199] op_sel_hi:[1,0]
	v_pk_mul_f32 v[32:33], v[32:33], v[198:199] op_sel_hi:[1,0]
	v_pk_mul_f32 v[30:31], v[30:31], v[198:199] op_sel_hi:[1,0]
	v_pk_mul_f32 v[54:55], v[28:29], v[198:199] op_sel_hi:[1,0]
	v_pk_mul_f32 v[50:51], v[26:27], v[198:199] op_sel_hi:[1,0]
	v_cvt_pk_bf16_f32 v26, v46, v47
	v_cvt_pk_bf16_f32 v27, v48, v49
	v_cvt_pk_bf16_f32 v28, v42, v43
	v_cvt_pk_bf16_f32 v29, v44, v45
	global_store_dwordx4 v[52:53], v[26:29], off
	s_nop 1
	v_cvt_pk_bf16_f32 v26, v30, v31
	v_cvt_pk_bf16_f32 v27, v32, v33
	v_cvt_pk_bf16_f32 v28, v50, v51
	v_cvt_pk_bf16_f32 v29, v54, v55
	global_store_dwordx4 v[52:53], v[26:29], off offset:256
	s_or_b64 exec, exec, s[24:25]
	s_nop 0
	s_nop 0
	v_cmp_lt_i32_e32 vcc, -1, v200
	s_and_saveexec_b64 s[24:25], vcc
	s_nop 0
	v_lshlrev_b64 v[28:29], 12, v[200:201]
	v_mov_b32_e32 v145, v139
	v_lshl_add_u64 v[28:29], s[8:9], 0, v[28:29]
	v_lshl_add_u64 v[28:29], v[28:29], 0, v[144:145]
	s_nop 0
	v_pk_mul_f32 v[30:31], v[12:13], v[202:203] op_sel_hi:[1,0]
	v_pk_mul_f32 v[12:13], v[10:11], v[202:203] op_sel_hi:[1,0]
	v_pk_mul_f32 v[16:17], v[16:17], v[202:203] op_sel_hi:[1,0]
	v_pk_mul_f32 v[14:15], v[14:15], v[202:203] op_sel_hi:[1,0]
	v_pk_mul_f32 v[32:33], v[36:37], v[202:203] op_sel_hi:[1,0]
	v_cvt_pk_bf16_f32 v10, v14, v15
	v_cvt_pk_bf16_f32 v11, v16, v17
	v_cvt_pk_bf16_f32 v12, v12, v13
	v_cvt_pk_bf16_f32 v13, v30, v31
	v_pk_mul_f32 v[34:35], v[34:35], v[202:203] op_sel_hi:[1,0]
	v_pk_mul_f32 v[36:37], v[40:41], v[202:203] op_sel_hi:[1,0]
	v_pk_mul_f32 v[26:27], v[38:39], v[202:203] op_sel_hi:[1,0]
	global_store_dwordx4 v[28:29], v[10:13], off
	s_nop 1
	v_cvt_pk_bf16_f32 v10, v34, v35
	v_cvt_pk_bf16_f32 v11, v32, v33
	v_cvt_pk_bf16_f32 v12, v26, v27
	v_cvt_pk_bf16_f32 v13, v36, v37
	global_store_dwordx4 v[28:29], v[10:13], off offset:256
	s_or_b64 exec, exec, s[24:25]
	s_nop 0
	s_nop 0
	v_cmp_lt_i32_e32 vcc, -1, v204
	s_and_saveexec_b64 s[24:25], vcc
	s_nop 0
	v_lshlrev_b64 v[12:13], 12, v[204:205]
	v_mov_b32_e32 v145, v139
	v_lshl_add_u64 v[12:13], s[8:9], 0, v[12:13]
	v_lshl_add_u64 v[12:13], v[12:13], 0, v[144:145]
	s_nop 0
	v_pk_mul_f32 v[14:15], v[4:5], v[206:207] op_sel_hi:[1,0]
	v_pk_mul_f32 v[4:5], v[2:3], v[206:207] op_sel_hi:[1,0]
	v_pk_mul_f32 v[8:9], v[8:9], v[206:207] op_sel_hi:[1,0]
	v_pk_mul_f32 v[6:7], v[6:7], v[206:207] op_sel_hi:[1,0]
	v_pk_mul_f32 v[16:17], v[20:21], v[206:207] op_sel_hi:[1,0]
	v_cvt_pk_bf16_f32 v2, v6, v7
	v_cvt_pk_bf16_f32 v3, v8, v9
	v_cvt_pk_bf16_f32 v4, v4, v5
	v_cvt_pk_bf16_f32 v5, v14, v15
	v_pk_mul_f32 v[18:19], v[18:19], v[206:207] op_sel_hi:[1,0]
	v_pk_mul_f32 v[20:21], v[24:25], v[206:207] op_sel_hi:[1,0]
	v_pk_mul_f32 v[10:11], v[22:23], v[206:207] op_sel_hi:[1,0]
	global_store_dwordx4 v[12:13], v[2:5], off
	s_nop 1
	v_cvt_pk_bf16_f32 v2, v18, v19
	v_cvt_pk_bf16_f32 v3, v16, v17
	v_cvt_pk_bf16_f32 v4, v10, v11
	v_cvt_pk_bf16_f32 v5, v20, v21
	global_store_dwordx4 v[12:13], v[2:5], off offset:256
	s_or_b64 exec, exec, s[24:25]
	s_andn2_b64 vcc, exec, s[18:19]
	s_mov_b64 s[18:19], -1
	s_cbranch_vccnz .LBB0_992
	s_andn2_b64 vcc, exec, s[2:3]
	s_cbranch_vccnz .LBB0_991
	s_barrier
	s_branch .LBB0_991
